# v049 + P7/P16: leading wave half runs its swiglu epilogue before (not after) its align barrier, so the two halves' epilogues run one after the other, each alone on the SIMD
# baseline (speedup 1.0000x reference)
.LBB0_786:
	v_pk_mul_f32 v[156:157], v[126:127], s[44:45] op_sel_hi:[1,0]
	v_pk_mul_f32 v[122:123], v[126:127], v[122:123]
	v_exp_f32_e32 v156, v156
	v_exp_f32_e32 v157, v157
	v_pk_mul_f32 v[126:127], v[118:119], s[44:45] op_sel_hi:[1,0]
	v_pk_mul_f32 v[158:159], v[128:129], s[44:45] op_sel_hi:[1,0]
	v_exp_f32_e32 v126, v126
	v_exp_f32_e32 v127, v127
	v_pk_fma_f32 v[156:157], v[156:157], s[50:51], s[50:51] op_sel_hi:[1,0,0]
	v_pk_mul_f32 v[124:125], v[128:129], v[124:125]
	v_pk_mul_f32 v[128:129], v[120:121], s[44:45] op_sel_hi:[1,0]
	v_exp_f32_e32 v158, v158
	v_exp_f32_e32 v159, v159
	v_rcp_f32_e32 v156, v156
	v_rcp_f32_e32 v157, v157
	v_exp_f32_e32 v128, v128
	v_exp_f32_e32 v129, v129
	v_pk_fma_f32 v[126:127], v[126:127], s[50:51], s[50:51] op_sel_hi:[1,0,0]
	v_pk_fma_f32 v[158:159], v[158:159], s[50:51], s[50:51] op_sel_hi:[1,0,0]
	v_rcp_f32_e32 v126, v126
	v_rcp_f32_e32 v127, v127
	v_pk_mul_f32 v[122:123], v[156:157], v[122:123]
	v_pk_fma_f32 v[128:129], v[128:129], s[50:51], s[50:51] op_sel_hi:[1,0,0]
	v_pk_mul_f32 v[114:115], v[118:119], v[114:115]
	v_rcp_f32_e32 v158, v158
	v_rcp_f32_e32 v159, v159
	v_rcp_f32_e32 v128, v128
	v_rcp_f32_e32 v129, v129
	v_pk_mul_f32 v[116:117], v[120:121], v[116:117]
	v_pk_mul_f32 v[114:115], v[126:127], v[114:115]
	v_med3_f32 v119, v122, s80, v154
	v_med3_f32 v120, v123, s80, v154
	v_cvt_pk_fp8_f32 v118, v119, v120
	v_med3_f32 v114, v114, s80, v154
	v_med3_f32 v115, v115, s80, v154
	v_cvt_pk_fp8_f32 v119, v114, v115
	v_pk_mul_f32 v[124:125], v[158:159], v[124:125]
	v_pk_mul_f32 v[116:117], v[128:129], v[116:117]
	v_med3_f32 v120, v124, s80, v154
	v_med3_f32 v121, v125, s80, v154
	v_med3_f32 v114, v116, s80, v154
	v_med3_f32 v115, v117, s80, v154
	v_cvt_pk_fp8_f32 v118, v120, v121 op_sel:[0,0,1]
	v_cvt_pk_fp8_f32 v119, v114, v115 op_sel:[0,0,1]
	v_lshl_add_u32 v155, s60, 8, v148
	v_lshl_or_b32 v144, s2, 7, v150
	v_mov_b64_e32 v[146:147], s[14:15]
	v_ashrrev_i32_e32 v145, 31, v144
	v_mad_i64_i32 v[114:115], s[26:27], v155, s75, v[146:147]
	v_lshl_add_u64 v[114:115], v[114:115], 0, v[144:145]
	global_store_dwordx2 v[114:115], v[118:119], off
	v_pk_mul_f32 v[114:115], v[110:111], s[44:45] op_sel_hi:[1,0]
	v_pk_mul_f32 v[106:107], v[110:111], v[106:107]
	v_exp_f32_e32 v114, v114
	v_exp_f32_e32 v115, v115
	v_pk_mul_f32 v[110:111], v[102:103], s[44:45] op_sel_hi:[1,0]
	v_pk_mul_f32 v[116:117], v[112:113], s[44:45] op_sel_hi:[1,0]
	v_exp_f32_e32 v110, v110
	v_exp_f32_e32 v111, v111
	v_pk_fma_f32 v[114:115], v[114:115], s[50:51], s[50:51] op_sel_hi:[1,0,0]
	v_pk_mul_f32 v[108:109], v[112:113], v[108:109]
	v_pk_mul_f32 v[112:113], v[104:105], s[44:45] op_sel_hi:[1,0]
	v_exp_f32_e32 v116, v116
	v_exp_f32_e32 v117, v117
	v_rcp_f32_e32 v114, v114
	v_rcp_f32_e32 v115, v115
	v_exp_f32_e32 v112, v112
	v_exp_f32_e32 v113, v113
	v_pk_fma_f32 v[110:111], v[110:111], s[50:51], s[50:51] op_sel_hi:[1,0,0]
	v_pk_fma_f32 v[116:117], v[116:117], s[50:51], s[50:51] op_sel_hi:[1,0,0]
	v_rcp_f32_e32 v110, v110
	v_rcp_f32_e32 v111, v111
	v_pk_mul_f32 v[106:107], v[114:115], v[106:107]
	v_pk_fma_f32 v[112:113], v[112:113], s[50:51], s[50:51] op_sel_hi:[1,0,0]
	v_pk_mul_f32 v[98:99], v[102:103], v[98:99]
	v_rcp_f32_e32 v116, v116
	v_rcp_f32_e32 v117, v117
	v_rcp_f32_e32 v112, v112
	v_rcp_f32_e32 v113, v113
	v_pk_mul_f32 v[100:101], v[104:105], v[100:101]
	v_pk_mul_f32 v[98:99], v[110:111], v[98:99]
	v_med3_f32 v103, v106, s80, v154
	v_med3_f32 v104, v107, s80, v154
	v_cvt_pk_fp8_f32 v102, v103, v104
	v_med3_f32 v98, v98, s80, v154
	v_med3_f32 v99, v99, s80, v154
	v_cvt_pk_fp8_f32 v103, v98, v99
	v_pk_mul_f32 v[108:109], v[116:117], v[108:109]
	v_pk_mul_f32 v[100:101], v[112:113], v[100:101]
	v_med3_f32 v104, v108, s80, v154
	v_med3_f32 v105, v109, s80, v154
	v_med3_f32 v98, v100, s80, v154
	v_med3_f32 v99, v101, s80, v154
	v_cvt_pk_fp8_f32 v102, v104, v105 op_sel:[0,0,1]
	v_cvt_pk_fp8_f32 v103, v98, v99 op_sel:[0,0,1]
	v_or_b32_e32 v118, 16, v155
	v_mad_i64_i32 v[98:99], s[26:27], v118, s75, v[146:147]
	v_lshl_add_u64 v[98:99], v[98:99], 0, v[144:145]
	global_store_dwordx2 v[98:99], v[102:103], off
	v_pk_mul_f32 v[98:99], v[94:95], s[44:45] op_sel_hi:[1,0]
	v_pk_mul_f32 v[90:91], v[94:95], v[90:91]
	v_exp_f32_e32 v98, v98
	v_exp_f32_e32 v99, v99
	v_pk_mul_f32 v[94:95], v[86:87], s[44:45] op_sel_hi:[1,0]
	v_pk_mul_f32 v[100:101], v[96:97], s[44:45] op_sel_hi:[1,0]
	v_exp_f32_e32 v94, v94
	v_exp_f32_e32 v95, v95
	v_pk_fma_f32 v[98:99], v[98:99], s[50:51], s[50:51] op_sel_hi:[1,0,0]
	v_pk_mul_f32 v[92:93], v[96:97], v[92:93]
	v_pk_mul_f32 v[96:97], v[88:89], s[44:45] op_sel_hi:[1,0]
	v_exp_f32_e32 v100, v100
	v_exp_f32_e32 v101, v101
	v_rcp_f32_e32 v98, v98
	v_rcp_f32_e32 v99, v99
	v_exp_f32_e32 v96, v96
	v_exp_f32_e32 v97, v97
	v_pk_fma_f32 v[94:95], v[94:95], s[50:51], s[50:51] op_sel_hi:[1,0,0]
	v_pk_fma_f32 v[100:101], v[100:101], s[50:51], s[50:51] op_sel_hi:[1,0,0]
	v_rcp_f32_e32 v94, v94
	v_rcp_f32_e32 v95, v95
	v_pk_mul_f32 v[90:91], v[98:99], v[90:91]
	v_pk_fma_f32 v[96:97], v[96:97], s[50:51], s[50:51] op_sel_hi:[1,0,0]
	v_pk_mul_f32 v[82:83], v[86:87], v[82:83]
	v_rcp_f32_e32 v100, v100
	v_rcp_f32_e32 v101, v101
	v_rcp_f32_e32 v96, v96
	v_rcp_f32_e32 v97, v97
	v_pk_mul_f32 v[84:85], v[88:89], v[84:85]
	v_pk_mul_f32 v[82:83], v[94:95], v[82:83]
	v_med3_f32 v87, v90, s80, v154
	v_med3_f32 v88, v91, s80, v154
	v_cvt_pk_fp8_f32 v86, v87, v88
	v_med3_f32 v82, v82, s80, v154
	v_med3_f32 v83, v83, s80, v154
	v_cvt_pk_fp8_f32 v87, v82, v83
	v_pk_mul_f32 v[92:93], v[100:101], v[92:93]
	v_pk_mul_f32 v[84:85], v[96:97], v[84:85]
	v_med3_f32 v88, v92, s80, v154
	v_med3_f32 v89, v93, s80, v154
	v_med3_f32 v82, v84, s80, v154
	v_med3_f32 v83, v85, s80, v154
	v_cvt_pk_fp8_f32 v86, v88, v89 op_sel:[0,0,1]
	v_cvt_pk_fp8_f32 v87, v82, v83 op_sel:[0,0,1]
	v_or_b32_e32 v102, 32, v155
	v_mad_i64_i32 v[82:83], s[26:27], v102, s75, v[146:147]
	v_lshl_add_u64 v[82:83], v[82:83], 0, v[144:145]
	global_store_dwordx2 v[82:83], v[86:87], off
	v_pk_mul_f32 v[82:83], v[78:79], s[44:45] op_sel_hi:[1,0]
	v_pk_mul_f32 v[74:75], v[78:79], v[74:75]
	v_exp_f32_e32 v82, v82
	v_exp_f32_e32 v83, v83
	v_pk_mul_f32 v[78:79], v[70:71], s[44:45] op_sel_hi:[1,0]
	v_pk_mul_f32 v[84:85], v[80:81], s[44:45] op_sel_hi:[1,0]
	v_exp_f32_e32 v78, v78
	v_exp_f32_e32 v79, v79
	v_pk_fma_f32 v[82:83], v[82:83], s[50:51], s[50:51] op_sel_hi:[1,0,0]
	v_pk_mul_f32 v[76:77], v[80:81], v[76:77]
	v_pk_mul_f32 v[80:81], v[72:73], s[44:45] op_sel_hi:[1,0]
	v_exp_f32_e32 v84, v84
	v_exp_f32_e32 v85, v85
	v_rcp_f32_e32 v82, v82
	v_rcp_f32_e32 v83, v83
	v_exp_f32_e32 v80, v80
	v_exp_f32_e32 v81, v81
	v_pk_fma_f32 v[78:79], v[78:79], s[50:51], s[50:51] op_sel_hi:[1,0,0]
	v_pk_fma_f32 v[84:85], v[84:85], s[50:51], s[50:51] op_sel_hi:[1,0,0]
	v_rcp_f32_e32 v78, v78
	v_rcp_f32_e32 v79, v79
	v_pk_mul_f32 v[74:75], v[82:83], v[74:75]
	v_pk_fma_f32 v[80:81], v[80:81], s[50:51], s[50:51] op_sel_hi:[1,0,0]
	v_pk_mul_f32 v[66:67], v[70:71], v[66:67]
	v_rcp_f32_e32 v84, v84
	v_rcp_f32_e32 v85, v85
	v_rcp_f32_e32 v80, v80
	v_rcp_f32_e32 v81, v81
	v_pk_mul_f32 v[68:69], v[72:73], v[68:69]
	v_pk_mul_f32 v[66:67], v[78:79], v[66:67]
	v_med3_f32 v71, v74, s80, v154
	v_med3_f32 v72, v75, s80, v154
	v_cvt_pk_fp8_f32 v70, v71, v72
	v_med3_f32 v66, v66, s80, v154
	v_med3_f32 v67, v67, s80, v154
	v_cvt_pk_fp8_f32 v71, v66, v67
	v_pk_mul_f32 v[76:77], v[84:85], v[76:77]
	v_pk_mul_f32 v[68:69], v[80:81], v[68:69]
	v_med3_f32 v72, v76, s80, v154
	v_med3_f32 v73, v77, s80, v154
	v_med3_f32 v66, v68, s80, v154
	v_med3_f32 v67, v69, s80, v154
	v_cvt_pk_fp8_f32 v70, v72, v73 op_sel:[0,0,1]
	v_cvt_pk_fp8_f32 v71, v66, v67 op_sel:[0,0,1]
	v_or_b32_e32 v86, 48, v155
	v_mad_i64_i32 v[66:67], s[26:27], v86, s75, v[146:147]
	v_lshl_add_u64 v[66:67], v[66:67], 0, v[144:145]
	global_store_dwordx2 v[66:67], v[70:71], off
	v_pk_mul_f32 v[66:67], v[62:63], s[44:45] op_sel_hi:[1,0]
	v_pk_mul_f32 v[58:59], v[62:63], v[58:59]
	v_exp_f32_e32 v66, v66
	v_exp_f32_e32 v67, v67
	v_pk_mul_f32 v[62:63], v[54:55], s[44:45] op_sel_hi:[1,0]
	v_pk_mul_f32 v[68:69], v[64:65], s[44:45] op_sel_hi:[1,0]
	v_exp_f32_e32 v62, v62
	v_exp_f32_e32 v63, v63
	v_pk_fma_f32 v[66:67], v[66:67], s[50:51], s[50:51] op_sel_hi:[1,0,0]
	v_pk_mul_f32 v[60:61], v[64:65], v[60:61]
	v_pk_mul_f32 v[64:65], v[56:57], s[44:45] op_sel_hi:[1,0]
	v_exp_f32_e32 v68, v68
	v_exp_f32_e32 v69, v69
	v_rcp_f32_e32 v66, v66
	v_rcp_f32_e32 v67, v67
	v_exp_f32_e32 v64, v64
	v_exp_f32_e32 v65, v65
	v_pk_fma_f32 v[62:63], v[62:63], s[50:51], s[50:51] op_sel_hi:[1,0,0]
	v_pk_fma_f32 v[68:69], v[68:69], s[50:51], s[50:51] op_sel_hi:[1,0,0]
	v_rcp_f32_e32 v62, v62
	v_rcp_f32_e32 v63, v63
	v_pk_mul_f32 v[58:59], v[66:67], v[58:59]
	v_pk_fma_f32 v[64:65], v[64:65], s[50:51], s[50:51] op_sel_hi:[1,0,0]
	v_pk_mul_f32 v[50:51], v[54:55], v[50:51]
	v_rcp_f32_e32 v68, v68
	v_rcp_f32_e32 v69, v69
	v_rcp_f32_e32 v64, v64
	v_rcp_f32_e32 v65, v65
	v_pk_mul_f32 v[52:53], v[56:57], v[52:53]
	v_pk_mul_f32 v[50:51], v[62:63], v[50:51]
	v_med3_f32 v55, v58, s80, v154
	v_med3_f32 v56, v59, s80, v154
	v_cvt_pk_fp8_f32 v54, v55, v56
	v_med3_f32 v50, v50, s80, v154
	v_med3_f32 v51, v51, s80, v154
	v_cvt_pk_fp8_f32 v55, v50, v51
	v_pk_mul_f32 v[60:61], v[68:69], v[60:61]
	v_pk_mul_f32 v[52:53], v[64:65], v[52:53]
	v_med3_f32 v56, v60, s80, v154
	v_med3_f32 v57, v61, s80, v154
	v_med3_f32 v50, v52, s80, v154
	v_med3_f32 v51, v53, s80, v154
	v_cvt_pk_fp8_f32 v54, v56, v57 op_sel:[0,0,1]
	v_cvt_pk_fp8_f32 v55, v50, v51 op_sel:[0,0,1]
	v_add_u32_e32 v70, 0x80, v155
	v_mad_i64_i32 v[50:51], s[26:27], v70, s75, v[146:147]
	v_lshl_add_u64 v[50:51], v[50:51], 0, v[144:145]
	global_store_dwordx2 v[50:51], v[54:55], off
	v_pk_mul_f32 v[50:51], v[46:47], s[44:45] op_sel_hi:[1,0]
	v_pk_mul_f32 v[42:43], v[46:47], v[42:43]
	v_exp_f32_e32 v50, v50
	v_exp_f32_e32 v51, v51
	v_pk_mul_f32 v[46:47], v[38:39], s[44:45] op_sel_hi:[1,0]
	v_pk_mul_f32 v[52:53], v[48:49], s[44:45] op_sel_hi:[1,0]
	v_exp_f32_e32 v46, v46
	v_exp_f32_e32 v47, v47
	v_pk_fma_f32 v[50:51], v[50:51], s[50:51], s[50:51] op_sel_hi:[1,0,0]
	v_pk_mul_f32 v[44:45], v[48:49], v[44:45]
	v_pk_mul_f32 v[48:49], v[40:41], s[44:45] op_sel_hi:[1,0]
	v_exp_f32_e32 v52, v52
	v_exp_f32_e32 v53, v53
	v_rcp_f32_e32 v50, v50
	v_rcp_f32_e32 v51, v51
	v_exp_f32_e32 v48, v48
	v_exp_f32_e32 v49, v49
	v_pk_fma_f32 v[46:47], v[46:47], s[50:51], s[50:51] op_sel_hi:[1,0,0]
	v_pk_fma_f32 v[52:53], v[52:53], s[50:51], s[50:51] op_sel_hi:[1,0,0]
	v_rcp_f32_e32 v46, v46
	v_rcp_f32_e32 v47, v47
	v_pk_mul_f32 v[42:43], v[50:51], v[42:43]
	v_pk_fma_f32 v[48:49], v[48:49], s[50:51], s[50:51] op_sel_hi:[1,0,0]
	v_pk_mul_f32 v[34:35], v[38:39], v[34:35]
	v_rcp_f32_e32 v52, v52
	v_rcp_f32_e32 v53, v53
	v_rcp_f32_e32 v48, v48
	v_rcp_f32_e32 v49, v49
	v_pk_mul_f32 v[36:37], v[40:41], v[36:37]
	v_pk_mul_f32 v[34:35], v[46:47], v[34:35]
	v_med3_f32 v39, v42, s80, v154
	v_med3_f32 v40, v43, s80, v154
	v_cvt_pk_fp8_f32 v38, v39, v40
	v_med3_f32 v34, v34, s80, v154
	v_med3_f32 v35, v35, s80, v154
	v_cvt_pk_fp8_f32 v39, v34, v35
	v_pk_mul_f32 v[44:45], v[52:53], v[44:45]
	v_pk_mul_f32 v[36:37], v[48:49], v[36:37]
	v_med3_f32 v40, v44, s80, v154
	v_med3_f32 v41, v45, s80, v154
	v_med3_f32 v34, v36, s80, v154
	v_med3_f32 v35, v37, s80, v154
	v_cvt_pk_fp8_f32 v38, v40, v41 op_sel:[0,0,1]
	v_cvt_pk_fp8_f32 v39, v34, v35 op_sel:[0,0,1]
	v_add_u32_e32 v54, 0x90, v155
	v_mad_i64_i32 v[34:35], s[26:27], v54, s75, v[146:147]
	v_lshl_add_u64 v[34:35], v[34:35], 0, v[144:145]
	global_store_dwordx2 v[34:35], v[38:39], off
	v_pk_mul_f32 v[34:35], v[30:31], s[44:45] op_sel_hi:[1,0]
	v_pk_mul_f32 v[26:27], v[30:31], v[26:27]
	v_exp_f32_e32 v34, v34
	v_exp_f32_e32 v35, v35
	v_pk_mul_f32 v[30:31], v[22:23], s[44:45] op_sel_hi:[1,0]
	v_pk_mul_f32 v[36:37], v[32:33], s[44:45] op_sel_hi:[1,0]
	v_exp_f32_e32 v30, v30
	v_exp_f32_e32 v31, v31
	v_pk_fma_f32 v[34:35], v[34:35], s[50:51], s[50:51] op_sel_hi:[1,0,0]
	v_pk_mul_f32 v[28:29], v[32:33], v[28:29]
	v_pk_mul_f32 v[32:33], v[24:25], s[44:45] op_sel_hi:[1,0]
	v_exp_f32_e32 v36, v36
	v_exp_f32_e32 v37, v37
	v_rcp_f32_e32 v34, v34
	v_rcp_f32_e32 v35, v35
	v_exp_f32_e32 v32, v32
	v_exp_f32_e32 v33, v33
	v_pk_fma_f32 v[30:31], v[30:31], s[50:51], s[50:51] op_sel_hi:[1,0,0]
	v_pk_fma_f32 v[36:37], v[36:37], s[50:51], s[50:51] op_sel_hi:[1,0,0]
	v_rcp_f32_e32 v30, v30
	v_rcp_f32_e32 v31, v31
	v_pk_mul_f32 v[26:27], v[34:35], v[26:27]
	v_pk_fma_f32 v[32:33], v[32:33], s[50:51], s[50:51] op_sel_hi:[1,0,0]
	v_pk_mul_f32 v[18:19], v[22:23], v[18:19]
	v_rcp_f32_e32 v36, v36
	v_rcp_f32_e32 v37, v37
	v_rcp_f32_e32 v32, v32
	v_rcp_f32_e32 v33, v33
	v_pk_mul_f32 v[20:21], v[24:25], v[20:21]
	v_pk_mul_f32 v[18:19], v[30:31], v[18:19]
	v_med3_f32 v23, v26, s80, v154
	v_med3_f32 v24, v27, s80, v154
	v_cvt_pk_fp8_f32 v22, v23, v24
	v_med3_f32 v18, v18, s80, v154
	v_med3_f32 v19, v19, s80, v154
	v_cvt_pk_fp8_f32 v23, v18, v19
	v_pk_mul_f32 v[28:29], v[36:37], v[28:29]
	v_pk_mul_f32 v[20:21], v[32:33], v[20:21]
	v_med3_f32 v24, v28, s80, v154
	v_med3_f32 v25, v29, s80, v154
	v_med3_f32 v18, v20, s80, v154
	v_med3_f32 v19, v21, s80, v154
	v_cvt_pk_fp8_f32 v22, v24, v25 op_sel:[0,0,1]
	v_cvt_pk_fp8_f32 v23, v18, v19 op_sel:[0,0,1]
	v_add_u32_e32 v38, 0xa0, v155
	v_mad_i64_i32 v[18:19], s[26:27], v38, s75, v[146:147]
	v_lshl_add_u64 v[18:19], v[18:19], 0, v[144:145]
	global_store_dwordx2 v[18:19], v[22:23], off
	v_pk_mul_f32 v[18:19], v[14:15], s[44:45] op_sel_hi:[1,0]
	v_pk_mul_f32 v[10:11], v[14:15], v[10:11]
	v_exp_f32_e32 v18, v18
	v_exp_f32_e32 v19, v19
	v_pk_mul_f32 v[14:15], v[6:7], s[44:45] op_sel_hi:[1,0]
	v_pk_mul_f32 v[20:21], v[16:17], s[44:45] op_sel_hi:[1,0]
	v_exp_f32_e32 v14, v14
	v_exp_f32_e32 v15, v15
	v_pk_fma_f32 v[18:19], v[18:19], s[50:51], s[50:51] op_sel_hi:[1,0,0]
	v_pk_mul_f32 v[12:13], v[16:17], v[12:13]
	v_pk_mul_f32 v[16:17], v[8:9], s[44:45] op_sel_hi:[1,0]
	v_exp_f32_e32 v20, v20
	v_exp_f32_e32 v21, v21
	v_rcp_f32_e32 v18, v18
	v_rcp_f32_e32 v19, v19
	v_exp_f32_e32 v16, v16
	v_exp_f32_e32 v17, v17
	v_pk_fma_f32 v[14:15], v[14:15], s[50:51], s[50:51] op_sel_hi:[1,0,0]
	v_pk_fma_f32 v[20:21], v[20:21], s[50:51], s[50:51] op_sel_hi:[1,0,0]
	v_rcp_f32_e32 v14, v14
	v_rcp_f32_e32 v15, v15
	v_pk_mul_f32 v[10:11], v[18:19], v[10:11]
	v_pk_fma_f32 v[16:17], v[16:17], s[50:51], s[50:51] op_sel_hi:[1,0,0]
	v_pk_mul_f32 v[2:3], v[6:7], v[2:3]
	v_rcp_f32_e32 v20, v20
	v_rcp_f32_e32 v21, v21
	v_rcp_f32_e32 v16, v16
	v_rcp_f32_e32 v17, v17
	v_pk_mul_f32 v[4:5], v[8:9], v[4:5]
	v_pk_mul_f32 v[2:3], v[14:15], v[2:3]
	v_med3_f32 v7, v10, s80, v154
	v_med3_f32 v8, v11, s80, v154
	v_cvt_pk_fp8_f32 v6, v7, v8
	v_med3_f32 v2, v2, s80, v154
	v_med3_f32 v3, v3, s80, v154
	v_cvt_pk_fp8_f32 v7, v2, v3
	v_pk_mul_f32 v[12:13], v[20:21], v[12:13]
	v_pk_mul_f32 v[4:5], v[16:17], v[4:5]
	v_med3_f32 v8, v12, s80, v154
	v_med3_f32 v9, v13, s80, v154
	v_med3_f32 v2, v4, s80, v154
	v_med3_f32 v3, v5, s80, v154
	v_cvt_pk_fp8_f32 v6, v8, v9 op_sel:[0,0,1]
	v_cvt_pk_fp8_f32 v7, v2, v3 op_sel:[0,0,1]
	v_add_u32_e32 v22, 0xb0, v155
	v_mad_i64_i32 v[2:3], s[26:27], v22, s75, v[146:147]
	v_lshl_add_u64 v[2:3], v[2:3], 0, v[144:145]
	s_and_b64 vcc, exec, s[40:41]
	s_cbranch_vccz .Llate_align_1
	s_barrier
.Llate_align_1:
	s_andn2_b64 vcc, exec, s[0:1]
	s_mov_b64 s[0:1], -1
	global_store_dwordx2 v[2:3], v[6:7], off
	s_cbranch_vccnz .LBB0_779
	s_andn2_b64 vcc, exec, s[12:13]
	s_cbranch_vccnz .LBB0_778
	s_barrier
	s_branch .LBB0_778

.LBB0_1500:
	v_pk_mul_f32 v[10:11], v[160:161], s[42:43] op_sel_hi:[1,0]
	v_pk_mul_f32 v[8:9], v[158:159], s[42:43] op_sel_hi:[1,0]
	v_exp_f32_e32 v10, v10
	v_exp_f32_e32 v11, v11
	v_exp_f32_e32 v8, v8
	v_exp_f32_e32 v9, v9
	v_pk_mul_f32 v[12:13], v[160:161], v[156:157]
	v_pk_fma_f32 v[10:11], v[10:11], s[44:45], s[44:45] op_sel_hi:[1,0,0]
	v_pk_mul_f32 v[14:15], v[158:159], v[154:155]
	v_rcp_f32_e32 v10, v10
	v_rcp_f32_e32 v11, v11
	v_pk_fma_f32 v[8:9], v[8:9], s[44:45], s[44:45] op_sel_hi:[1,0,0]
	v_pk_mul_f32 v[18:19], v[150:151], v[146:147]
	v_rcp_f32_e32 v8, v8
	v_rcp_f32_e32 v9, v9
	v_pk_mul_f32 v[10:11], v[12:13], v[10:11]
	v_pk_mul_f32 v[12:13], v[150:151], s[42:43] op_sel_hi:[1,0]
	v_pk_mul_f32 v[16:17], v[152:153], v[148:149]
	v_exp_f32_e32 v12, v12
	v_exp_f32_e32 v13, v13
	v_pk_mul_f32 v[8:9], v[14:15], v[8:9]
	v_pk_mul_f32 v[14:15], v[152:153], s[42:43] op_sel_hi:[1,0]
	v_med3_f32 v7, v8, s72, v191
	v_exp_f32_e32 v14, v14
	v_exp_f32_e32 v15, v15
	v_pk_fma_f32 v[12:13], v[12:13], s[44:45], s[44:45] op_sel_hi:[1,0,0]
	v_med3_f32 v9, v9, s72, v191
	v_rcp_f32_e32 v12, v12
	v_rcp_f32_e32 v13, v13
	v_pk_fma_f32 v[14:15], v[14:15], s[44:45], s[44:45] op_sel_hi:[1,0,0]
	v_rcp_f32_e32 v14, v14
	v_rcp_f32_e32 v15, v15
	v_pk_mul_f32 v[12:13], v[18:19], v[12:13]
	v_cvt_pk_fp8_f32 v8, v7, v9
	v_med3_f32 v7, v10, s72, v191
	v_med3_f32 v10, v11, s72, v191
	v_med3_f32 v11, v12, s72, v191
	v_med3_f32 v12, v13, s72, v191
	v_cvt_pk_fp8_f32 v9, v11, v12
	v_pk_mul_f32 v[14:15], v[16:17], v[14:15]
	v_readlane_b32 s4, v254, 56
	v_cvt_pk_fp8_f32 v8, v7, v10 op_sel:[0,0,1]
	v_med3_f32 v7, v14, s72, v191
	v_med3_f32 v10, v15, s72, v191
	v_readlane_b32 s5, v254, 57
	v_cvt_pk_fp8_f32 v9, v7, v10 op_sel:[0,0,1]
	v_lshl_add_u32 v6, s54, 8, v1
	v_lshl_or_b32 v2, s52, 7, v185
	v_mov_b64_e32 v[4:5], s[4:5]
	v_ashrrev_i32_e32 v3, 31, v2
	v_mad_i64_i32 v[10:11], s[4:5], v6, s71, v[4:5]
	v_lshl_add_u64 v[10:11], v[10:11], 0, v[2:3]
	s_nop 15
	s_nop 15
	global_store_dwordx2 v[10:11], v[8:9], off
	v_pk_mul_f32 v[8:9], v[142:143], s[42:43] op_sel_hi:[1,0]
	v_pk_mul_f32 v[10:11], v[144:145], s[42:43] op_sel_hi:[1,0]
	v_exp_f32_e32 v8, v8
	v_exp_f32_e32 v9, v9
	v_exp_f32_e32 v10, v10
	v_exp_f32_e32 v11, v11
	v_pk_mul_f32 v[12:13], v[144:145], v[140:141]
	v_pk_fma_f32 v[8:9], v[8:9], s[44:45], s[44:45] op_sel_hi:[1,0,0]
	v_pk_mul_f32 v[14:15], v[142:143], v[138:139]
	v_pk_fma_f32 v[10:11], v[10:11], s[44:45], s[44:45] op_sel_hi:[1,0,0]
	v_rcp_f32_e32 v8, v8
	v_rcp_f32_e32 v9, v9
	v_rcp_f32_e32 v10, v10
	v_rcp_f32_e32 v11, v11
	v_pk_mul_f32 v[16:17], v[136:137], v[132:133]
	v_pk_mul_f32 v[8:9], v[14:15], v[8:9]
	v_pk_mul_f32 v[14:15], v[136:137], s[42:43] op_sel_hi:[1,0]
	v_pk_mul_f32 v[10:11], v[12:13], v[10:11]
	v_pk_mul_f32 v[12:13], v[134:135], s[42:43] op_sel_hi:[1,0]
	v_exp_f32_e32 v14, v14
	v_exp_f32_e32 v12, v12
	v_exp_f32_e32 v13, v13
	v_exp_f32_e32 v15, v15
	v_pk_mul_f32 v[18:19], v[134:135], v[130:131]
	v_med3_f32 v9, v9, s72, v191
	v_pk_fma_f32 v[12:13], v[12:13], s[44:45], s[44:45] op_sel_hi:[1,0,0]
	v_pk_fma_f32 v[14:15], v[14:15], s[44:45], s[44:45] op_sel_hi:[1,0,0]
	v_rcp_f32_e32 v12, v12
	v_rcp_f32_e32 v13, v13
	v_rcp_f32_e32 v14, v14
	v_rcp_f32_e32 v15, v15
	v_med3_f32 v10, v10, s72, v191
	v_pk_mul_f32 v[12:13], v[18:19], v[12:13]
	v_med3_f32 v11, v11, s72, v191
	v_pk_mul_f32 v[14:15], v[16:17], v[14:15]
	v_med3_f32 v16, v8, s72, v191
	v_cvt_pk_fp8_f32 v8, v16, v9
	v_med3_f32 v12, v12, s72, v191
	v_med3_f32 v13, v13, s72, v191
	v_cvt_pk_fp8_f32 v9, v12, v13
	v_cvt_pk_fp8_f32 v8, v10, v11 op_sel:[0,0,1]
	v_med3_f32 v10, v14, s72, v191
	v_med3_f32 v11, v15, s72, v191
	v_cvt_pk_fp8_f32 v9, v10, v11 op_sel:[0,0,1]
	v_or_b32_e32 v7, 16, v6
	v_mad_i64_i32 v[10:11], s[4:5], v7, s71, v[4:5]
	v_lshl_add_u64 v[10:11], v[10:11], 0, v[2:3]
	global_store_dwordx2 v[10:11], v[8:9], off
	v_pk_mul_f32 v[8:9], v[126:127], s[42:43] op_sel_hi:[1,0]
	v_pk_mul_f32 v[10:11], v[128:129], s[42:43] op_sel_hi:[1,0]
	v_exp_f32_e32 v8, v8
	v_exp_f32_e32 v9, v9
	v_exp_f32_e32 v10, v10
	v_exp_f32_e32 v11, v11
	v_pk_mul_f32 v[12:13], v[128:129], v[124:125]
	v_pk_fma_f32 v[8:9], v[8:9], s[44:45], s[44:45] op_sel_hi:[1,0,0]
	v_pk_mul_f32 v[14:15], v[126:127], v[122:123]
	v_pk_fma_f32 v[10:11], v[10:11], s[44:45], s[44:45] op_sel_hi:[1,0,0]
	v_rcp_f32_e32 v8, v8
	v_rcp_f32_e32 v9, v9
	v_rcp_f32_e32 v10, v10
	v_rcp_f32_e32 v11, v11
	v_pk_mul_f32 v[16:17], v[120:121], v[116:117]
	v_pk_mul_f32 v[8:9], v[14:15], v[8:9]
	v_pk_mul_f32 v[14:15], v[120:121], s[42:43] op_sel_hi:[1,0]
	v_pk_mul_f32 v[10:11], v[12:13], v[10:11]
	v_pk_mul_f32 v[12:13], v[118:119], s[42:43] op_sel_hi:[1,0]
	v_exp_f32_e32 v14, v14
	v_exp_f32_e32 v12, v12
	v_exp_f32_e32 v13, v13
	v_exp_f32_e32 v15, v15
	v_pk_mul_f32 v[18:19], v[118:119], v[114:115]
	v_med3_f32 v9, v9, s72, v191
	v_pk_fma_f32 v[12:13], v[12:13], s[44:45], s[44:45] op_sel_hi:[1,0,0]
	v_pk_fma_f32 v[14:15], v[14:15], s[44:45], s[44:45] op_sel_hi:[1,0,0]
	v_rcp_f32_e32 v12, v12
	v_rcp_f32_e32 v13, v13
	v_rcp_f32_e32 v14, v14
	v_rcp_f32_e32 v15, v15
	v_med3_f32 v10, v10, s72, v191
	v_pk_mul_f32 v[12:13], v[18:19], v[12:13]
	v_med3_f32 v11, v11, s72, v191
	v_pk_mul_f32 v[14:15], v[16:17], v[14:15]
	v_med3_f32 v16, v8, s72, v191
	v_cvt_pk_fp8_f32 v8, v16, v9
	v_med3_f32 v12, v12, s72, v191
	v_med3_f32 v13, v13, s72, v191
	v_cvt_pk_fp8_f32 v9, v12, v13
	v_cvt_pk_fp8_f32 v8, v10, v11 op_sel:[0,0,1]
	v_med3_f32 v10, v14, s72, v191
	v_med3_f32 v11, v15, s72, v191
	v_cvt_pk_fp8_f32 v9, v10, v11 op_sel:[0,0,1]
	v_or_b32_e32 v7, 32, v6
	v_mad_i64_i32 v[10:11], s[4:5], v7, s71, v[4:5]
	v_lshl_add_u64 v[10:11], v[10:11], 0, v[2:3]
	global_store_dwordx2 v[10:11], v[8:9], off
	v_pk_mul_f32 v[8:9], v[110:111], s[42:43] op_sel_hi:[1,0]
	v_pk_mul_f32 v[10:11], v[112:113], s[42:43] op_sel_hi:[1,0]
	v_exp_f32_e32 v8, v8
	v_exp_f32_e32 v9, v9
	v_exp_f32_e32 v10, v10
	v_exp_f32_e32 v11, v11
	v_pk_mul_f32 v[12:13], v[112:113], v[108:109]
	v_pk_fma_f32 v[8:9], v[8:9], s[44:45], s[44:45] op_sel_hi:[1,0,0]
	v_pk_mul_f32 v[14:15], v[110:111], v[106:107]
	v_pk_fma_f32 v[10:11], v[10:11], s[44:45], s[44:45] op_sel_hi:[1,0,0]
	v_rcp_f32_e32 v8, v8
	v_rcp_f32_e32 v9, v9
	v_rcp_f32_e32 v10, v10
	v_rcp_f32_e32 v11, v11
	v_pk_mul_f32 v[16:17], v[104:105], v[100:101]
	v_pk_mul_f32 v[8:9], v[14:15], v[8:9]
	v_pk_mul_f32 v[14:15], v[104:105], s[42:43] op_sel_hi:[1,0]
	v_pk_mul_f32 v[10:11], v[12:13], v[10:11]
	v_pk_mul_f32 v[12:13], v[102:103], s[42:43] op_sel_hi:[1,0]
	v_exp_f32_e32 v14, v14
	v_exp_f32_e32 v12, v12
	v_exp_f32_e32 v13, v13
	v_exp_f32_e32 v15, v15
	v_pk_mul_f32 v[18:19], v[102:103], v[98:99]
	v_med3_f32 v9, v9, s72, v191
	v_pk_fma_f32 v[12:13], v[12:13], s[44:45], s[44:45] op_sel_hi:[1,0,0]
	v_pk_fma_f32 v[14:15], v[14:15], s[44:45], s[44:45] op_sel_hi:[1,0,0]
	v_rcp_f32_e32 v12, v12
	v_rcp_f32_e32 v13, v13
	v_rcp_f32_e32 v14, v14
	v_rcp_f32_e32 v15, v15
	v_med3_f32 v10, v10, s72, v191
	v_pk_mul_f32 v[12:13], v[18:19], v[12:13]
	v_med3_f32 v11, v11, s72, v191
	v_pk_mul_f32 v[14:15], v[16:17], v[14:15]
	v_med3_f32 v16, v8, s72, v191
	v_cvt_pk_fp8_f32 v8, v16, v9
	v_med3_f32 v12, v12, s72, v191
	v_med3_f32 v13, v13, s72, v191
	v_cvt_pk_fp8_f32 v9, v12, v13
	v_cvt_pk_fp8_f32 v8, v10, v11 op_sel:[0,0,1]
	v_med3_f32 v10, v14, s72, v191
	v_med3_f32 v11, v15, s72, v191
	v_cvt_pk_fp8_f32 v9, v10, v11 op_sel:[0,0,1]
	v_or_b32_e32 v7, 48, v6
	v_mad_i64_i32 v[10:11], s[4:5], v7, s71, v[4:5]
	v_lshl_add_u64 v[10:11], v[10:11], 0, v[2:3]
	global_store_dwordx2 v[10:11], v[8:9], off
	v_pk_mul_f32 v[8:9], v[94:95], s[42:43] op_sel_hi:[1,0]
	v_pk_mul_f32 v[10:11], v[96:97], s[42:43] op_sel_hi:[1,0]
	v_exp_f32_e32 v8, v8
	v_exp_f32_e32 v9, v9
	v_exp_f32_e32 v10, v10
	v_exp_f32_e32 v11, v11
	v_pk_mul_f32 v[12:13], v[96:97], v[92:93]
	v_pk_fma_f32 v[8:9], v[8:9], s[44:45], s[44:45] op_sel_hi:[1,0,0]
	v_pk_mul_f32 v[14:15], v[94:95], v[90:91]
	v_pk_fma_f32 v[10:11], v[10:11], s[44:45], s[44:45] op_sel_hi:[1,0,0]
	v_rcp_f32_e32 v8, v8
	v_rcp_f32_e32 v9, v9
	v_rcp_f32_e32 v10, v10
	v_rcp_f32_e32 v11, v11
	v_pk_mul_f32 v[16:17], v[88:89], v[84:85]
	v_pk_mul_f32 v[8:9], v[14:15], v[8:9]
	v_pk_mul_f32 v[14:15], v[88:89], s[42:43] op_sel_hi:[1,0]
	v_pk_mul_f32 v[10:11], v[12:13], v[10:11]
	v_pk_mul_f32 v[12:13], v[86:87], s[42:43] op_sel_hi:[1,0]
	v_exp_f32_e32 v14, v14
	v_exp_f32_e32 v12, v12
	v_exp_f32_e32 v13, v13
	v_exp_f32_e32 v15, v15
	v_pk_mul_f32 v[18:19], v[86:87], v[82:83]
	v_med3_f32 v9, v9, s72, v191
	v_pk_fma_f32 v[12:13], v[12:13], s[44:45], s[44:45] op_sel_hi:[1,0,0]
	v_pk_fma_f32 v[14:15], v[14:15], s[44:45], s[44:45] op_sel_hi:[1,0,0]
	v_rcp_f32_e32 v12, v12
	v_rcp_f32_e32 v13, v13
	v_rcp_f32_e32 v14, v14
	v_rcp_f32_e32 v15, v15
	v_med3_f32 v10, v10, s72, v191
	v_pk_mul_f32 v[12:13], v[18:19], v[12:13]
	v_med3_f32 v11, v11, s72, v191
	v_pk_mul_f32 v[14:15], v[16:17], v[14:15]
	v_med3_f32 v16, v8, s72, v191
	v_cvt_pk_fp8_f32 v8, v16, v9
	v_med3_f32 v12, v12, s72, v191
	v_med3_f32 v13, v13, s72, v191
	v_cvt_pk_fp8_f32 v9, v12, v13
	v_cvt_pk_fp8_f32 v8, v10, v11 op_sel:[0,0,1]
	v_med3_f32 v10, v14, s72, v191
	v_med3_f32 v11, v15, s72, v191
	v_cvt_pk_fp8_f32 v9, v10, v11 op_sel:[0,0,1]
	v_add_u32_e32 v7, 0x80, v6
	v_mad_i64_i32 v[10:11], s[4:5], v7, s71, v[4:5]
	v_lshl_add_u64 v[10:11], v[10:11], 0, v[2:3]
	global_store_dwordx2 v[10:11], v[8:9], off
	v_pk_mul_f32 v[8:9], v[78:79], s[42:43] op_sel_hi:[1,0]
	v_pk_mul_f32 v[10:11], v[80:81], s[42:43] op_sel_hi:[1,0]
	v_exp_f32_e32 v8, v8
	v_exp_f32_e32 v9, v9
	v_exp_f32_e32 v10, v10
	v_exp_f32_e32 v11, v11
	v_pk_mul_f32 v[12:13], v[80:81], v[76:77]
	v_pk_fma_f32 v[8:9], v[8:9], s[44:45], s[44:45] op_sel_hi:[1,0,0]
	v_pk_mul_f32 v[14:15], v[78:79], v[74:75]
	v_pk_fma_f32 v[10:11], v[10:11], s[44:45], s[44:45] op_sel_hi:[1,0,0]
	v_rcp_f32_e32 v8, v8
	v_rcp_f32_e32 v9, v9
	v_rcp_f32_e32 v10, v10
	v_rcp_f32_e32 v11, v11
	v_pk_mul_f32 v[16:17], v[72:73], v[68:69]
	v_pk_mul_f32 v[8:9], v[14:15], v[8:9]
	v_pk_mul_f32 v[14:15], v[72:73], s[42:43] op_sel_hi:[1,0]
	v_pk_mul_f32 v[10:11], v[12:13], v[10:11]
	v_pk_mul_f32 v[12:13], v[70:71], s[42:43] op_sel_hi:[1,0]
	v_exp_f32_e32 v14, v14
	v_exp_f32_e32 v12, v12
	v_exp_f32_e32 v13, v13
	v_exp_f32_e32 v15, v15
	v_pk_mul_f32 v[18:19], v[70:71], v[66:67]
	v_med3_f32 v9, v9, s72, v191
	v_pk_fma_f32 v[12:13], v[12:13], s[44:45], s[44:45] op_sel_hi:[1,0,0]
	v_pk_fma_f32 v[14:15], v[14:15], s[44:45], s[44:45] op_sel_hi:[1,0,0]
	v_rcp_f32_e32 v12, v12
	v_rcp_f32_e32 v13, v13
	v_rcp_f32_e32 v14, v14
	v_rcp_f32_e32 v15, v15
	v_med3_f32 v10, v10, s72, v191
	v_pk_mul_f32 v[12:13], v[18:19], v[12:13]
	v_med3_f32 v11, v11, s72, v191
	v_pk_mul_f32 v[14:15], v[16:17], v[14:15]
	v_med3_f32 v16, v8, s72, v191
	v_cvt_pk_fp8_f32 v8, v16, v9
	v_med3_f32 v12, v12, s72, v191
	v_med3_f32 v13, v13, s72, v191
	v_cvt_pk_fp8_f32 v9, v12, v13
	v_cvt_pk_fp8_f32 v8, v10, v11 op_sel:[0,0,1]
	v_med3_f32 v10, v14, s72, v191
	v_med3_f32 v11, v15, s72, v191
	v_cvt_pk_fp8_f32 v9, v10, v11 op_sel:[0,0,1]
	v_add_u32_e32 v7, 0x90, v6
	v_mad_i64_i32 v[10:11], s[4:5], v7, s71, v[4:5]
	v_lshl_add_u64 v[10:11], v[10:11], 0, v[2:3]
	global_store_dwordx2 v[10:11], v[8:9], off
	v_pk_mul_f32 v[8:9], v[62:63], s[42:43] op_sel_hi:[1,0]
	v_pk_mul_f32 v[10:11], v[64:65], s[42:43] op_sel_hi:[1,0]
	v_exp_f32_e32 v8, v8
	v_exp_f32_e32 v9, v9
	v_exp_f32_e32 v10, v10
	v_exp_f32_e32 v11, v11
	v_pk_mul_f32 v[12:13], v[64:65], v[60:61]
	v_pk_fma_f32 v[8:9], v[8:9], s[44:45], s[44:45] op_sel_hi:[1,0,0]
	v_pk_mul_f32 v[14:15], v[62:63], v[58:59]
	v_pk_fma_f32 v[10:11], v[10:11], s[44:45], s[44:45] op_sel_hi:[1,0,0]
	v_rcp_f32_e32 v8, v8
	v_rcp_f32_e32 v9, v9
	v_rcp_f32_e32 v10, v10
	v_rcp_f32_e32 v11, v11
	v_pk_mul_f32 v[16:17], v[56:57], v[52:53]
	v_pk_mul_f32 v[8:9], v[14:15], v[8:9]
	v_pk_mul_f32 v[14:15], v[56:57], s[42:43] op_sel_hi:[1,0]
	v_pk_mul_f32 v[10:11], v[12:13], v[10:11]
	v_pk_mul_f32 v[12:13], v[54:55], s[42:43] op_sel_hi:[1,0]
	v_exp_f32_e32 v14, v14
	v_exp_f32_e32 v12, v12
	v_exp_f32_e32 v13, v13
	v_exp_f32_e32 v15, v15
	v_pk_mul_f32 v[18:19], v[54:55], v[50:51]
	v_med3_f32 v9, v9, s72, v191
	v_pk_fma_f32 v[12:13], v[12:13], s[44:45], s[44:45] op_sel_hi:[1,0,0]
	v_pk_fma_f32 v[14:15], v[14:15], s[44:45], s[44:45] op_sel_hi:[1,0,0]
	v_rcp_f32_e32 v12, v12
	v_rcp_f32_e32 v13, v13
	v_rcp_f32_e32 v14, v14
	v_rcp_f32_e32 v15, v15
	v_med3_f32 v10, v10, s72, v191
	v_pk_mul_f32 v[12:13], v[18:19], v[12:13]
	v_med3_f32 v11, v11, s72, v191
	v_pk_mul_f32 v[14:15], v[16:17], v[14:15]
	v_med3_f32 v16, v8, s72, v191
	v_cvt_pk_fp8_f32 v8, v16, v9
	v_med3_f32 v12, v12, s72, v191
	v_med3_f32 v13, v13, s72, v191
	v_cvt_pk_fp8_f32 v9, v12, v13
	v_cvt_pk_fp8_f32 v8, v10, v11 op_sel:[0,0,1]
	v_med3_f32 v10, v14, s72, v191
	v_med3_f32 v11, v15, s72, v191
	v_cvt_pk_fp8_f32 v9, v10, v11 op_sel:[0,0,1]
	v_add_u32_e32 v7, 0xa0, v6
	v_mad_i64_i32 v[10:11], s[4:5], v7, s71, v[4:5]
	v_lshl_add_u64 v[10:11], v[10:11], 0, v[2:3]
	global_store_dwordx2 v[10:11], v[8:9], off
	v_add_u32_e32 v18, 0xb0, v6
	v_pk_mul_f32 v[6:7], v[46:47], s[42:43] op_sel_hi:[1,0]
	v_pk_mul_f32 v[8:9], v[48:49], s[42:43] op_sel_hi:[1,0]
	v_exp_f32_e32 v6, v6
	v_exp_f32_e32 v7, v7
	v_exp_f32_e32 v8, v8
	v_exp_f32_e32 v9, v9
	v_pk_mul_f32 v[10:11], v[48:49], v[44:45]
	v_pk_fma_f32 v[6:7], v[6:7], s[44:45], s[44:45] op_sel_hi:[1,0,0]
	v_pk_mul_f32 v[12:13], v[46:47], v[42:43]
	v_pk_fma_f32 v[8:9], v[8:9], s[44:45], s[44:45] op_sel_hi:[1,0,0]
	v_rcp_f32_e32 v6, v6
	v_rcp_f32_e32 v7, v7
	v_rcp_f32_e32 v8, v8
	v_rcp_f32_e32 v9, v9
	v_pk_mul_f32 v[14:15], v[40:41], v[36:37]
	v_pk_mul_f32 v[6:7], v[12:13], v[6:7]
	v_pk_mul_f32 v[12:13], v[40:41], s[42:43] op_sel_hi:[1,0]
	v_pk_mul_f32 v[8:9], v[10:11], v[8:9]
	v_pk_mul_f32 v[10:11], v[38:39], s[42:43] op_sel_hi:[1,0]
	v_exp_f32_e32 v12, v12
	v_exp_f32_e32 v10, v10
	v_exp_f32_e32 v11, v11
	v_exp_f32_e32 v13, v13
	v_pk_mul_f32 v[16:17], v[38:39], v[34:35]
	v_med3_f32 v7, v7, s72, v191
	v_pk_fma_f32 v[10:11], v[10:11], s[44:45], s[44:45] op_sel_hi:[1,0,0]
	v_pk_fma_f32 v[12:13], v[12:13], s[44:45], s[44:45] op_sel_hi:[1,0,0]
	v_rcp_f32_e32 v10, v10
	v_rcp_f32_e32 v11, v11
	v_rcp_f32_e32 v12, v12
	v_rcp_f32_e32 v13, v13
	v_med3_f32 v8, v8, s72, v191
	v_pk_mul_f32 v[10:11], v[16:17], v[10:11]
	v_med3_f32 v9, v9, s72, v191
	v_pk_mul_f32 v[12:13], v[14:15], v[12:13]
	v_med3_f32 v14, v6, s72, v191
	v_cvt_pk_fp8_f32 v6, v14, v7
	v_med3_f32 v10, v10, s72, v191
	v_med3_f32 v11, v11, s72, v191
	v_cvt_pk_fp8_f32 v7, v10, v11
	v_cvt_pk_fp8_f32 v6, v8, v9 op_sel:[0,0,1]
	v_med3_f32 v8, v12, s72, v191
	v_med3_f32 v9, v13, s72, v191
	v_cvt_pk_fp8_f32 v7, v8, v9 op_sel:[0,0,1]
	v_mad_i64_i32 v[4:5], s[4:5], v18, s71, v[4:5]
	v_lshl_add_u64 v[2:3], v[4:5], 0, v[2:3]
	s_and_b64 vcc, exec, s[38:39]
	s_cbranch_vccz .Llate_align_0
	s_barrier
.Llate_align_0:
	s_and_b64 vcc, exec, s[0:1]
	s_mov_b64 s[0:1], -1
	global_store_dwordx2 v[2:3], v[6:7], off
	s_cbranch_vccnz .LBB0_1487
	s_andn2_b64 vcc, exec, s[18:19]
	s_cbranch_vccnz .LBB0_1486
	s_barrier
	s_branch .LBB0_1486
